# gemm_unit_scheduler_div_by_group_size_4_fastpath
# speedup vs baseline: 1.0099x; 1.0099x over previous
.LBB0_249:
	s_add_i32 s55, s55, 1
	s_mul_i32 s2, s55, s54
	s_mul_hi_u32 s3, s55, s28
	s_add_i32 s3, s3, s2
	s_mul_i32 s2, s55, s28
	s_add_u32 s26, s2, s29
	s_addc_u32 s27, s3, s39
	v_mov_b64_e32 v[2:3], 0x580
	v_cmp_lt_i64_e64 s[2:3], s[26:27], v[2:3]
	v_mov_b64_e32 v[2:3], 0x57f
	v_cmp_gt_i64_e32 vcc, s[26:27], v[2:3]
	s_cbranch_vccnz .LBB0_251
	s_ashr_i32 s20, s26, 31
	s_lshr_b32 s20, s20, 29
	s_add_i32 s20, s26, s20
	s_ashr_i32 s21, s20, 3
	s_and_b32 s20, s20, -8
	s_sub_i32 s20, s26, s20
	s_cmp_lt_i32 s20, 0
	s_movk_i32 s22, 0xb1
	s_cselect_b32 s22, s22, 0xb0
	s_mul_i32 s20, s22, s20
	s_add_i32 s20, s20, s21
	s_mul_hi_i32 s21, s20, 0x2e8ba2e9
	s_lshr_b32 s22, s21, 31
	s_ashr_i32 s21, s21, 3
	s_add_i32 s21, s21, s22
	s_lshl_b32 s22, s21, 2
	s_sub_i32 s23, 0x80, s22
	s_min_i32 s23, s23, 4
	s_abs_i32 s25, s23
	v_cvt_f32_u32_e32 v2, s25
	s_sub_i32 s27, 0, s25
	s_mul_i32 s21, s21, 44
	s_sub_i32 s21, s20, s21
	v_rcp_iflag_f32_e32 v2, v2
	s_abs_i32 s20, s21
	s_xor_b32 s26, s21, s23
	s_ashr_i32 s26, s26, 31
	s_cmp_eq_u32 s23, 4
	s_cbranch_scc0 .Lhd_slow_0
	s_ashr_i32 s20, s21, 2
	s_branch .Lhd_done_0
.Lhd_slow_0:
	v_mul_f32_e32 v2, 0x4f7ffffe, v2
	v_cvt_u32_f32_e32 v2, v2
	s_nop 0
	v_readfirstlane_b32 s59, v2
	s_mul_i32 s27, s27, s59
	s_mul_hi_u32 s27, s59, s27
	s_add_i32 s59, s59, s27
	s_mul_hi_u32 s27, s20, s59
	s_mul_i32 s59, s27, s25
	s_sub_i32 s20, s20, s59
	s_add_i32 s60, s27, 1
	s_sub_i32 s59, s20, s25
	s_cmp_ge_u32 s20, s25
	s_cselect_b32 s27, s60, s27
	s_cselect_b32 s20, s59, s20
	s_add_i32 s59, s27, 1
	s_cmp_ge_u32 s20, s25
	s_cselect_b32 s20, s59, s27
	s_xor_b32 s20, s20, s26
	s_sub_i32 s20, s20, s26
.Lhd_done_0:
	s_mul_i32 s23, s20, s23
	s_sub_i32 s21, s21, s23
	s_add_i32 s22, s21, s22

.LBB0_572:
	s_ashr_i32 s2, s16, 3
	s_add_i32 s2, s18, s2
	s_ashr_i32 s3, s2, 31
	s_lshr_b32 s3, s3, 28
	s_add_i32 s3, s2, s3
	s_ashr_i32 s16, s3, 4
	s_lshl_b32 s16, s16, 2
	s_sub_i32 s17, 0x80, s16
	s_min_i32 s17, s17, 4
	s_abs_i32 s18, s17
	v_cvt_f32_u32_e32 v2, s18
	s_sub_i32 s20, 0, s18
	s_and_b32 s3, s3, -16
	s_sub_i32 s2, s2, s3
	v_rcp_iflag_f32_e32 v2, v2
	s_abs_i32 s3, s2
	s_xor_b32 s19, s2, s17
	s_ashr_i32 s19, s19, 31
	s_cmp_eq_u32 s17, 4
	s_cbranch_scc0 .Lhd_slow_1
	s_ashr_i32 s54, s2, 2
	s_branch .Lhd_done_1
.Lhd_slow_1:
	v_mul_f32_e32 v2, 0x4f7ffffe, v2
	v_cvt_u32_f32_e32 v2, v2
	s_nop 0
	v_readfirstlane_b32 s21, v2
	s_mul_i32 s20, s20, s21
	s_mul_hi_u32 s20, s21, s20
	s_add_i32 s21, s21, s20
	s_mul_hi_u32 s20, s3, s21
	s_mul_i32 s21, s20, s18
	s_sub_i32 s3, s3, s21
	s_add_i32 s22, s20, 1
	s_sub_i32 s21, s3, s18
	s_cmp_ge_u32 s3, s18
	s_cselect_b32 s20, s22, s20
	s_cselect_b32 s3, s21, s3
	s_add_i32 s21, s20, 1
	s_cmp_ge_u32 s3, s18
	s_cselect_b32 s3, s21, s20
	s_xor_b32 s3, s3, s19
	s_sub_i32 s54, s3, s19
.Lhd_done_1:
	s_mul_i32 s3, s54, s17
	s_sub_i32 s2, s2, s3
	s_add_i32 s55, s16, s2

.LBB0_659:
	s_ashr_i32 s16, s18, 3
	s_add_i32 s16, s22, s16
	s_ashr_i32 s17, s16, 31
	s_lshr_b32 s17, s17, 28
	s_add_i32 s17, s16, s17
	s_ashr_i32 s18, s17, 4
	s_lshl_b32 s18, s18, 2
	s_sub_i32 s19, 0x80, s18
	s_min_i32 s19, s19, 4
	s_abs_i32 s22, s19
	v_cvt_f32_u32_e32 v2, s22
	s_sub_i32 s52, 0, s22
	s_and_b32 s17, s17, -16
	s_sub_i32 s17, s16, s17
	v_rcp_iflag_f32_e32 v2, v2
	s_abs_i32 s16, s17
	s_xor_b32 s23, s17, s19
	s_ashr_i32 s23, s23, 31
	s_cmp_eq_u32 s19, 4
	s_cbranch_scc0 .Lhd_slow_2
	s_ashr_i32 s16, s17, 2
	s_branch .Lhd_done_2
.Lhd_slow_2:
	v_mul_f32_e32 v2, 0x4f7ffffe, v2
	v_cvt_u32_f32_e32 v2, v2
	s_nop 0
	v_readfirstlane_b32 s53, v2
	s_mul_i32 s52, s52, s53
	s_mul_hi_u32 s52, s53, s52
	s_add_i32 s53, s53, s52
	s_mul_hi_u32 s52, s16, s53
	s_mul_i32 s53, s52, s22
	s_sub_i32 s16, s16, s53
	s_add_i32 s54, s52, 1
	s_sub_i32 s53, s16, s22
	s_cmp_ge_u32 s16, s22
	s_cselect_b32 s52, s54, s52
	s_cselect_b32 s16, s53, s16
	s_add_i32 s53, s52, 1
	s_cmp_ge_u32 s16, s22
	s_cselect_b32 s16, s53, s52
	s_xor_b32 s16, s16, s23
	s_sub_i32 s16, s16, s23
.Lhd_done_2:
	s_mul_i32 s19, s16, s19
	s_sub_i32 s17, s17, s19
	s_add_i32 s18, s18, s17

.LBB0_953:
	s_add_i32 s57, s57, 1
	s_mul_i32 s0, s57, s56
	s_mul_hi_u32 s1, s57, s37
	s_add_i32 s1, s1, s0
	s_mul_i32 s0, s57, s37
	s_add_u32 s2, s0, s36
	s_addc_u32 s3, s1, s40
	v_mov_b64_e32 v[2:3], 0x1600
	v_cmp_lt_i64_e64 s[0:1], s[2:3], v[2:3]
	v_mov_b64_e32 v[2:3], 0x15ff
	v_cmp_gt_i64_e64 s[4:5], s[2:3], v[2:3]
	s_and_b64 vcc, exec, s[4:5]
	s_cbranch_vccnz .LBB0_955
	s_ashr_i32 s3, s2, 31
	s_lshr_b32 s3, s3, 29
	s_add_i32 s3, s2, s3
	s_ashr_i32 s18, s3, 3
	s_and_b32 s3, s3, -8
	s_sub_i32 s2, s2, s3
	s_cmp_lt_i32 s2, 0
	s_movk_i32 s3, 0x2c1
	s_cselect_b32 s3, s3, 0x2c0
	s_mul_i32 s2, s3, s2
	s_add_i32 s2, s2, s18
	s_mul_hi_i32 s3, s2, 0x2e8ba2e9
	s_lshr_b32 s18, s3, 31
	s_ashr_i32 s3, s3, 4
	s_add_i32 s3, s3, s18
	s_lshl_b32 s19, s3, 2
	s_sub_i32 s18, 0x100, s19
	s_min_i32 s22, s18, 4
	s_abs_i32 s18, s22
	v_cvt_f32_u32_e32 v2, s18
	s_sub_i32 s24, 0, s18
	s_mulk_i32 s3, 0x58
	s_sub_i32 s2, s2, s3
	v_rcp_iflag_f32_e32 v2, v2
	s_abs_i32 s3, s2
	s_xor_b32 s23, s2, s22
	s_ashr_i32 s23, s23, 31
	s_cmp_eq_u32 s22, 4
	s_cbranch_scc0 .Lhd_slow_3
	s_ashr_i32 s18, s2, 2
	s_branch .Lhd_done_3
.Lhd_slow_3:
	v_mul_f32_e32 v2, 0x4f7ffffe, v2
	v_cvt_u32_f32_e32 v2, v2
	s_nop 0
	v_readfirstlane_b32 s25, v2
	s_mul_i32 s24, s24, s25
	s_mul_hi_u32 s24, s25, s24
	s_add_i32 s25, s25, s24
	s_mul_hi_u32 s24, s3, s25
	s_mul_i32 s25, s24, s18
	s_sub_i32 s3, s3, s25
	s_add_i32 s26, s24, 1
	s_sub_i32 s25, s3, s18
	s_cmp_ge_u32 s3, s18
	s_cselect_b32 s24, s26, s24
	s_cselect_b32 s3, s25, s3
	s_add_i32 s25, s24, 1
	s_cmp_ge_u32 s3, s18
	s_cselect_b32 s3, s25, s24
	s_xor_b32 s3, s3, s23
	s_sub_i32 s18, s3, s23
.Lhd_done_3:
	s_mul_i32 s3, s18, s22
	s_sub_i32 s2, s2, s3
	s_add_i32 s58, s2, s19

.LBB0_1041:
	s_ashr_i32 s2, s16, 3
	s_add_i32 s2, s18, s2
	s_ashr_i32 s3, s2, 31
	s_lshr_b32 s3, s3, 28
	s_add_i32 s3, s2, s3
	s_ashr_i32 s16, s3, 4
	s_lshl_b32 s16, s16, 2
	s_sub_i32 s17, 0x100, s16
	s_min_i32 s17, s17, 4
	s_abs_i32 s18, s17
	v_cvt_f32_u32_e32 v2, s18
	s_sub_i32 s20, 0, s18
	s_and_b32 s3, s3, -16
	s_sub_i32 s2, s2, s3
	v_rcp_iflag_f32_e32 v2, v2
	s_abs_i32 s3, s2
	s_xor_b32 s19, s2, s17
	s_ashr_i32 s19, s19, 31
	s_cmp_eq_u32 s17, 4
	s_cbranch_scc0 .Lhd_slow_4
	s_ashr_i32 s51, s2, 2
	s_branch .Lhd_done_4
.Lhd_slow_4:
	v_mul_f32_e32 v2, 0x4f7ffffe, v2
	v_cvt_u32_f32_e32 v2, v2
	s_nop 0
	v_readfirstlane_b32 s21, v2
	s_mul_i32 s20, s20, s21
	s_mul_hi_u32 s20, s21, s20
	s_add_i32 s21, s21, s20
	s_mul_hi_u32 s20, s3, s21
	s_mul_i32 s21, s20, s18
	s_sub_i32 s3, s3, s21
	s_add_i32 s22, s20, 1
	s_sub_i32 s21, s3, s18
	s_cmp_ge_u32 s3, s18
	s_cselect_b32 s20, s22, s20
	s_cselect_b32 s3, s21, s3
	s_add_i32 s21, s20, 1
	s_cmp_ge_u32 s3, s18
	s_cselect_b32 s3, s21, s20
	s_xor_b32 s3, s3, s19
	s_sub_i32 s51, s3, s19
.Lhd_done_4:
	s_mul_i32 s3, s51, s17
	s_sub_i32 s2, s2, s3
	s_add_i32 s52, s16, s2
